# expert gate/up GEMM: tile bias fetched by LDS-DMA at K-loop start, epilogue reads it from LDS (no global loads / full vmcnt wait at the epilogue start)
# speedup vs baseline: 1.0018x; 1.0004x over previous
.LBB0_1430:
	s_ashr_i32 s41, s40, 31
	s_lshl_b64 s[44:45], s[40:41], 22
	s_add_u32 s21, s52, s44
	s_addc_u32 s31, s53, s45
	v_readlane_b32 s44, v253, 36
	v_readlane_b32 s45, v253, 37
	s_mov_b32 s48, s44
	s_ashr_i32 s49, s44, 31
	v_writelane_b32 v253, s44, 36
	v_mov_b32_e32 v66, 0
	s_mov_b32 s83, -2
	v_writelane_b32 v253, s45, 37
	s_lshl_b64 s[44:45], s[48:49], 19
	s_add_u32 s44, s21, s44
	s_addc_u32 s45, s31, s45
	s_and_b64 s[48:49], s[8:9], exec
	s_cselect_b32 s21, s45, s47
	s_cselect_b32 s41, s44, s46
	s_ashr_i32 s43, s42, 31
	s_lshl_b64 s[48:49], s[42:43], 10
	s_add_u32 s43, s46, 0x100
	v_lshl_add_u64 v[214:215], v[212:213], 0, s[48:49]
	s_addc_u32 s68, s47, 0
	s_mov_b64 s[46:47], s[34:35]
	v_mov_b32_e32 v67, v66
	v_mov_b32_e32 v68, v66
	v_mov_b32_e32 v69, v66
	v_mov_b32_e32 v74, v66
	v_mov_b32_e32 v75, v66
	v_mov_b32_e32 v76, v66
	v_mov_b32_e32 v77, v66
	v_mov_b32_e32 v82, v66
	v_mov_b32_e32 v83, v66
	v_mov_b32_e32 v84, v66
	v_mov_b32_e32 v85, v66
	v_mov_b32_e32 v90, v66
	v_mov_b32_e32 v91, v66
	v_mov_b32_e32 v92, v66
	v_mov_b32_e32 v93, v66
	v_mov_b32_e32 v100, v66
	v_mov_b32_e32 v101, v66
	v_mov_b32_e32 v102, v66
	v_mov_b32_e32 v103, v66
	v_mov_b32_e32 v108, v66
	v_mov_b32_e32 v109, v66
	v_mov_b32_e32 v110, v66
	v_mov_b32_e32 v111, v66
	v_mov_b32_e32 v116, v66
	v_mov_b32_e32 v117, v66
	v_mov_b32_e32 v118, v66
	v_mov_b32_e32 v119, v66
	v_mov_b32_e32 v124, v66
	v_mov_b32_e32 v125, v66
	v_mov_b32_e32 v126, v66
	v_mov_b32_e32 v127, v66
	v_mov_b32_e32 v70, v66
	v_mov_b32_e32 v71, v66
	v_mov_b32_e32 v72, v66
	v_mov_b32_e32 v73, v66
	v_mov_b32_e32 v78, v66
	v_mov_b32_e32 v79, v66
	v_mov_b32_e32 v80, v66
	v_mov_b32_e32 v81, v66
	v_mov_b32_e32 v86, v66
	v_mov_b32_e32 v87, v66
	v_mov_b32_e32 v88, v66
	v_mov_b32_e32 v89, v66
	v_mov_b32_e32 v94, v66
	v_mov_b32_e32 v95, v66
	v_mov_b32_e32 v96, v66
	v_mov_b32_e32 v97, v66
	v_mov_b32_e32 v104, v66
	v_mov_b32_e32 v105, v66
	v_mov_b32_e32 v106, v66
	v_mov_b32_e32 v107, v66
	v_mov_b32_e32 v112, v66
	v_mov_b32_e32 v113, v66
	v_mov_b32_e32 v114, v66
	v_mov_b32_e32 v115, v66
	v_mov_b32_e32 v120, v66
	v_mov_b32_e32 v121, v66
	v_mov_b32_e32 v122, v66
	v_mov_b32_e32 v123, v66
	v_mov_b32_e32 v128, v66
	v_mov_b32_e32 v129, v66
	v_mov_b32_e32 v130, v66
	v_mov_b32_e32 v131, v66
	v_mov_b32_e32 v132, v66
	v_mov_b32_e32 v133, v66
	v_mov_b32_e32 v134, v66
	v_mov_b32_e32 v135, v66
	v_mov_b32_e32 v140, v66
	v_mov_b32_e32 v141, v66
	v_mov_b32_e32 v142, v66
	v_mov_b32_e32 v143, v66
	v_mov_b32_e32 v148, v66
	v_mov_b32_e32 v149, v66
	v_mov_b32_e32 v150, v66
	v_mov_b32_e32 v151, v66
	v_mov_b32_e32 v156, v66
	v_mov_b32_e32 v157, v66
	v_mov_b32_e32 v158, v66
	v_mov_b32_e32 v159, v66
	v_mov_b32_e32 v164, v66
	v_mov_b32_e32 v165, v66
	v_mov_b32_e32 v166, v66
	v_mov_b32_e32 v167, v66
	v_mov_b32_e32 v172, v66
	v_mov_b32_e32 v173, v66
	v_mov_b32_e32 v174, v66
	v_mov_b32_e32 v175, v66
	v_mov_b32_e32 v180, v66
	v_mov_b32_e32 v181, v66
	v_mov_b32_e32 v182, v66
	v_mov_b32_e32 v183, v66
	v_mov_b32_e32 v188, v66
	v_mov_b32_e32 v189, v66
	v_mov_b32_e32 v190, v66
	v_mov_b32_e32 v191, v66
	v_mov_b32_e32 v136, v66
	v_mov_b32_e32 v137, v66
	v_mov_b32_e32 v138, v66
	v_mov_b32_e32 v139, v66
	v_mov_b32_e32 v144, v66
	v_mov_b32_e32 v145, v66
	v_mov_b32_e32 v146, v66
	v_mov_b32_e32 v147, v66
	v_mov_b32_e32 v152, v66
	v_mov_b32_e32 v153, v66
	v_mov_b32_e32 v154, v66
	v_mov_b32_e32 v155, v66
	v_mov_b32_e32 v160, v66
	v_mov_b32_e32 v161, v66
	v_mov_b32_e32 v162, v66
	v_mov_b32_e32 v163, v66
	v_mov_b32_e32 v168, v66
	v_mov_b32_e32 v169, v66
	v_mov_b32_e32 v170, v66
	v_mov_b32_e32 v171, v66
	v_mov_b32_e32 v176, v66
	v_mov_b32_e32 v177, v66
	v_mov_b32_e32 v178, v66
	v_mov_b32_e32 v179, v66
	v_mov_b32_e32 v184, v66
	v_mov_b32_e32 v185, v66
	v_mov_b32_e32 v186, v66
	v_mov_b32_e32 v187, v66
	v_mov_b32_e32 v192, v66
	v_mov_b32_e32 v193, v66
	v_mov_b32_e32 v194, v66
	v_mov_b32_e32 v195, v66
	v_mbcnt_lo_u32_b32 v3, -1, 0
	v_mbcnt_hi_u32_b32 v3, -1, v3
	v_readfirstlane_b32 s100, v0
	v_lshlrev_b32_e32 v3, 2, v3
	s_lshr_b32 s100, s100, 6
	s_cmp_gt_u32 s100, 3
	s_cbranch_scc1 .Lg1pf_skip
	s_and_b32 vcc_lo, s66, 1
	s_lshl_b32 vcc_lo, vcc_lo, 10
	s_add_i32 vcc_lo, vcc_lo, 0x21c00
	s_and_b32 vcc_hi, s100, 1
	s_lshl_b32 vcc_hi, vcc_hi, 8
	s_lshr_b32 s100, s100, 1
	s_lshl_b32 s101, s100, 9
	s_add_i32 m0, vcc_lo, vcc_hi
	s_add_i32 m0, m0, s101
	s_lshl_b32 s100, s100, 12
	s_add_i32 s100, s100, vcc_hi
	v_readlane_b32 s101, v253, 36
	s_lshl_b32 s101, s101, 9
	s_add_i32 s100, s100, s101
	s_lshl_b32 s101, s10, 13
	s_add_i32 s101, s101, s100
	s_add_u32 s100, s29, s101
	s_addc_u32 s101, s55, 0
	s_nop 0
	global_load_lds_dword v3, s[100:101]
.Lg1pf_skip:
	s_branch .LBB0_1433

.LBB0_1437:
	s_lshl_b32 s21, s11, 8
	s_ashr_i32 s11, s10, 31
	s_lshl_b64 s[10:11], s[10:11], 13
	s_add_u32 s31, s29, s10
	s_addc_u32 s41, s55, s11
	v_readlane_b32 s10, v253, 36
	v_readlane_b32 s11, v253, 37
	s_lshl_b32 s10, s10, 7
	s_ashr_i32 s11, s10, 31
	v_mov_b32_e32 v2, v216
	v_mov_b32_e32 v20, v201
	s_lshl_b64 s[46:47], s[10:11], 2
	s_add_u32 s46, s31, s46
	v_lshl_add_u32 v18, v2, 3, s13
	s_addc_u32 s47, s41, s47
	v_ashrrev_i32_e32 v19, 31, v18
	s_mov_b64 s[46:47], 0x1000
	s_add_i32 s21, s21, s56
	s_and_b32 s100, s66, 1
	s_lshl_b32 s100, s100, 10
	s_add_i32 s100, s100, 0x21c00
	s_lshl_b32 s101, s13, 2
	s_add_i32 s101, s101, s100
	v_lshl_add_u32 v6, v2, 5, s101
	ds_read_b128 v[2:5], v6 offset:16
	ds_read_b128 v[10:13], v6
	ds_read_b128 v[14:17], v6 offset:512
	ds_read_b128 v[6:9], v6 offset:528
	v_add_u32_e32 v20, s21, v20
	v_ashrrev_i32_e32 v21, 31, v20
	v_lshlrev_b64 v[20:21], 10, v[20:21]
	v_lshl_add_u64 v[20:21], s[80:81], 0, v[20:21]
	v_lshl_add_u64 v[20:21], v[20:21], 0, s[10:11]
	v_lshl_add_u64 v[18:19], v[20:21], 0, v[18:19]
	v_mov_b32_e32 v20, v99
	v_mov_b32_e32 v21, v99
	s_movk_i32 s10, 0x4000
	v_readlane_b32 s83, v255, 2
	s_waitcnt lgkmcnt(0)
	v_add_f32_e32 v22, v192, v10
	v_min_f32_e32 v22, 0x40e00000, v22
	v_add_f32_e32 v23, v188, v14
	v_med3_f32 v23, v23, s26, v236
	v_add_f32_e32 v23, 1.0, v23
	v_mul_f32_e32 v23, v22, v23
	v_mul_f32_e32 v22, 0xc01d265f, v22
	v_exp_f32_e32 v22, v22
	v_add_f32_e32 v24, v189, v15
	v_med3_f32 v24, v24, s26, v236
	v_add_f32_e32 v24, 1.0, v24
	v_add_f32_e32 v22, 1.0, v22
	v_rcp_f32_e32 v22, v22
	v_add_f32_e32 v25, v190, v16
	v_med3_f32 v25, v25, s26, v236
	v_add_f32_e32 v25, 1.0, v25
	v_mul_f32_e32 v22, v23, v22
	v_add_f32_e32 v23, v193, v11
	v_min_f32_e32 v23, 0x40e00000, v23
	v_mul_f32_e32 v24, v23, v24
	v_mul_f32_e32 v23, 0xc01d265f, v23
	v_exp_f32_e32 v23, v23
	v_add_f32_e32 v26, v191, v17
	v_med3_f32 v26, v26, s26, v236
	v_add_f32_e32 v26, 1.0, v26
	v_add_f32_e32 v23, 1.0, v23
	v_rcp_f32_e32 v23, v23
	v_add_f32_e32 v27, v180, v6
	v_med3_f32 v27, v27, s26, v236
	v_add_f32_e32 v27, 1.0, v27
	v_mul_f32_e32 v23, v24, v23
	v_add_f32_e32 v24, v194, v12
	v_min_f32_e32 v24, 0x40e00000, v24
	v_mul_f32_e32 v25, v24, v25
	v_mul_f32_e32 v24, 0xc01d265f, v24
	v_exp_f32_e32 v24, v24
	v_add_f32_e32 v28, v181, v7
	v_med3_f32 v28, v28, s26, v236
	v_add_f32_e32 v28, 1.0, v28
	v_add_f32_e32 v24, 1.0, v24
	v_rcp_f32_e32 v24, v24
	v_add_f32_e32 v29, v182, v8
	v_med3_f32 v29, v29, s26, v236
	v_add_f32_e32 v29, 1.0, v29
	v_mul_f32_e32 v24, v25, v24
	v_add_f32_e32 v25, v195, v13
	v_min_f32_e32 v25, 0x40e00000, v25
	v_mul_f32_e32 v26, v25, v26
	v_mul_f32_e32 v25, 0xc01d265f, v25
	v_exp_f32_e32 v25, v25
	v_add_f32_e32 v30, v183, v9
	v_med3_f32 v30, v30, s26, v236
	v_add_f32_e32 v30, 1.0, v30
	v_add_f32_e32 v25, 1.0, v25
	v_rcp_f32_e32 v25, v25
	v_cvt_pk_fp8_f32 v20, v22, v23
	v_add_f32_e32 v22, v173, v15
	v_med3_f32 v22, v22, s26, v236
	v_mul_f32_e32 v25, v26, v25
	v_add_f32_e32 v26, v184, v2
	v_min_f32_e32 v26, 0x40e00000, v26
	v_mul_f32_e32 v27, v26, v27
	v_mul_f32_e32 v26, 0xc01d265f, v26
	v_exp_f32_e32 v26, v26
	v_cvt_pk_fp8_f32 v20, v24, v25 op_sel:[0,0,1]
	v_add_f32_e32 v22, 1.0, v22
	v_add_f32_e32 v23, v174, v16
	v_add_f32_e32 v26, 1.0, v26
	v_rcp_f32_e32 v26, v26
	v_med3_f32 v23, v23, s26, v236
	v_add_f32_e32 v23, 1.0, v23
	v_add_f32_e32 v24, v175, v17
	v_mul_f32_e32 v26, v27, v26
	v_add_f32_e32 v27, v185, v3
	v_min_f32_e32 v27, 0x40e00000, v27
	v_mul_f32_e32 v28, v27, v28
	v_mul_f32_e32 v27, 0xc01d265f, v27
	v_exp_f32_e32 v27, v27
	v_med3_f32 v24, v24, s26, v236
	v_add_f32_e32 v24, 1.0, v24
	v_add_f32_e32 v25, v164, v6
	v_add_f32_e32 v27, 1.0, v27
	v_rcp_f32_e32 v27, v27
	v_med3_f32 v25, v25, s26, v236
	v_add_f32_e32 v25, 1.0, v25
	v_mul_f32_e32 v27, v28, v27
	v_add_f32_e32 v28, v186, v4
	v_min_f32_e32 v28, 0x40e00000, v28
	v_mul_f32_e32 v29, v28, v29
	v_mul_f32_e32 v28, 0xc01d265f, v28
	v_exp_f32_e32 v28, v28
	v_cvt_pk_fp8_f32 v21, v26, v27
	v_add_f32_e32 v26, v165, v7
	v_med3_f32 v26, v26, s26, v236
	v_add_f32_e32 v28, 1.0, v28
	v_rcp_f32_e32 v28, v28
	v_add_f32_e32 v26, 1.0, v26
	v_add_f32_e32 v27, v166, v8
	v_med3_f32 v27, v27, s26, v236
	v_mul_f32_e32 v28, v29, v28
	v_add_f32_e32 v29, v187, v5
	v_min_f32_e32 v29, 0x40e00000, v29
	v_mul_f32_e32 v30, v29, v30
	v_mul_f32_e32 v29, 0xc01d265f, v29
	v_exp_f32_e32 v29, v29
	v_add_f32_e32 v27, 1.0, v27
	v_add_f32_e32 v29, 1.0, v29
	v_rcp_f32_e32 v29, v29
	s_nop 0
	v_mul_f32_e32 v29, v30, v29
	v_cvt_pk_fp8_f32 v21, v28, v29 op_sel:[0,0,1]
	v_add_f32_e32 v28, v167, v9
	v_med3_f32 v28, v28, s26, v236
	v_add_f32_e32 v28, 1.0, v28
	global_store_dwordx2 v[18:19], v[20:21], off
	v_add_f32_e32 v21, v172, v14
	v_add_f32_e32 v20, v176, v10
	v_med3_f32 v21, v21, s26, v236
	v_min_f32_e32 v20, 0x40e00000, v20
	v_add_f32_e32 v21, 1.0, v21
	v_mul_f32_e32 v21, v20, v21
	v_mul_f32_e32 v20, 0xc01d265f, v20
	v_exp_f32_e32 v20, v20
	s_nop 0
	v_add_f32_e32 v20, 1.0, v20
	v_rcp_f32_e32 v20, v20
	s_nop 0
	v_mul_f32_e32 v21, v21, v20
	v_add_f32_e32 v20, v177, v11
	v_min_f32_e32 v20, 0x40e00000, v20
	v_mul_f32_e32 v22, v20, v22
	v_mul_f32_e32 v20, 0xc01d265f, v20
	v_exp_f32_e32 v20, v20
	s_nop 0
	v_add_f32_e32 v20, 1.0, v20
	v_rcp_f32_e32 v20, v20
	s_nop 0
	v_mul_f32_e32 v22, v22, v20
	v_add_f32_e32 v20, v178, v12
	v_min_f32_e32 v20, 0x40e00000, v20
	v_mul_f32_e32 v23, v20, v23
	v_mul_f32_e32 v20, 0xc01d265f, v20
	v_exp_f32_e32 v20, v20
	s_nop 0
	v_add_f32_e32 v20, 1.0, v20
	v_rcp_f32_e32 v20, v20
	s_nop 0
	v_mul_f32_e32 v23, v23, v20
	v_add_f32_e32 v20, v179, v13
	v_min_f32_e32 v20, 0x40e00000, v20
	v_mul_f32_e32 v24, v20, v24
	v_mul_f32_e32 v20, 0xc01d265f, v20
	v_exp_f32_e32 v20, v20
	s_nop 0
	v_add_f32_e32 v20, 1.0, v20
	v_rcp_f32_e32 v20, v20
	s_nop 0
	v_mul_f32_e32 v24, v24, v20
	v_add_f32_e32 v20, v168, v2
	v_min_f32_e32 v20, 0x40e00000, v20
	v_mul_f32_e32 v25, v20, v25
	v_mul_f32_e32 v20, 0xc01d265f, v20
	v_exp_f32_e32 v20, v20
	s_nop 0
	v_add_f32_e32 v20, 1.0, v20
	v_rcp_f32_e32 v20, v20
	s_nop 0
	v_mul_f32_e32 v25, v25, v20
	v_add_f32_e32 v20, v169, v3
	v_min_f32_e32 v20, 0x40e00000, v20
	v_mul_f32_e32 v26, v20, v26
	v_mul_f32_e32 v20, 0xc01d265f, v20
	v_exp_f32_e32 v20, v20
	s_nop 0
	v_add_f32_e32 v20, 1.0, v20
	v_rcp_f32_e32 v20, v20
	s_nop 0
	v_mul_f32_e32 v26, v26, v20
	v_add_f32_e32 v20, v170, v4
	v_min_f32_e32 v20, 0x40e00000, v20
	v_mul_f32_e32 v27, v20, v27
	v_mul_f32_e32 v20, 0xc01d265f, v20
	v_exp_f32_e32 v20, v20
	s_nop 0
	v_add_f32_e32 v20, 1.0, v20
	v_rcp_f32_e32 v20, v20
	s_nop 0
	v_mul_f32_e32 v27, v27, v20
	v_add_f32_e32 v20, v171, v5
	v_min_f32_e32 v20, 0x40e00000, v20
	v_mul_f32_e32 v28, v20, v28
	v_mul_f32_e32 v20, 0xc01d265f, v20
	v_exp_f32_e32 v20, v20
	s_nop 0
	v_add_f32_e32 v20, 1.0, v20
	v_rcp_f32_e32 v20, v20
	s_nop 0
	v_mul_f32_e32 v28, v28, v20
	v_mov_b32_e32 v20, v99
	v_cvt_pk_fp8_f32 v20, v21, v22
	v_mov_b32_e32 v21, v99
	v_cvt_pk_fp8_f32 v21, v25, v26
	v_add_co_u32_e32 v22, vcc, s10, v18
	v_cvt_pk_fp8_f32 v20, v23, v24 op_sel:[0,0,1]
	v_cvt_pk_fp8_f32 v21, v27, v28 op_sel:[0,0,1]
	v_addc_co_u32_e32 v23, vcc, 0, v19, vcc
	v_add_f32_e32 v24, v159, v17
	global_store_dwordx2 v[22:23], v[20:21], off
	v_add_f32_e32 v21, v156, v14
	v_add_f32_e32 v20, v160, v10
	v_med3_f32 v21, v21, s26, v236
	v_min_f32_e32 v20, 0x40e00000, v20
	v_add_f32_e32 v21, 1.0, v21
	v_mul_f32_e32 v21, v20, v21
	v_mul_f32_e32 v20, 0xc01d265f, v20
	v_exp_f32_e32 v20, v20
	v_add_f32_e32 v22, v157, v15
	v_med3_f32 v22, v22, s26, v236
	v_add_f32_e32 v22, 1.0, v22
	v_add_f32_e32 v20, 1.0, v20
	v_rcp_f32_e32 v20, v20
	v_add_f32_e32 v23, v158, v16
	v_med3_f32 v23, v23, s26, v236
	v_add_f32_e32 v23, 1.0, v23
	v_mul_f32_e32 v21, v21, v20
	v_add_f32_e32 v20, v161, v11
	v_min_f32_e32 v20, 0x40e00000, v20
	v_mul_f32_e32 v22, v20, v22
	v_mul_f32_e32 v20, 0xc01d265f, v20
	v_exp_f32_e32 v20, v20
	v_med3_f32 v24, v24, s26, v236
	v_add_f32_e32 v24, 1.0, v24
	v_add_f32_e32 v25, v148, v6
	v_add_f32_e32 v20, 1.0, v20
	v_rcp_f32_e32 v20, v20
	v_med3_f32 v25, v25, s26, v236
	v_add_f32_e32 v25, 1.0, v25
	v_add_f32_e32 v26, v149, v7
	v_mul_f32_e32 v22, v22, v20
	v_add_f32_e32 v20, v162, v12
	v_min_f32_e32 v20, 0x40e00000, v20
	v_mul_f32_e32 v23, v20, v23
	v_mul_f32_e32 v20, 0xc01d265f, v20
	v_exp_f32_e32 v20, v20
	v_med3_f32 v26, v26, s26, v236
	v_add_f32_e32 v26, 1.0, v26
	v_add_f32_e32 v27, v150, v8
	v_add_f32_e32 v20, 1.0, v20
	v_rcp_f32_e32 v20, v20
	v_med3_f32 v27, v27, s26, v236
	v_add_f32_e32 v27, 1.0, v27
	v_add_f32_e32 v28, v151, v9
	v_mul_f32_e32 v23, v23, v20
	v_add_f32_e32 v20, v163, v13
	v_min_f32_e32 v20, 0x40e00000, v20
	v_mul_f32_e32 v24, v20, v24
	v_mul_f32_e32 v20, 0xc01d265f, v20
	v_exp_f32_e32 v20, v20
	v_med3_f32 v28, v28, s26, v236
	v_add_f32_e32 v28, 1.0, v28
	s_mov_b32 s10, 0x8000
	v_add_f32_e32 v20, 1.0, v20
	v_rcp_f32_e32 v20, v20
	s_nop 0
	v_mul_f32_e32 v24, v24, v20
	v_add_f32_e32 v20, v152, v2
	v_min_f32_e32 v20, 0x40e00000, v20
	v_mul_f32_e32 v25, v20, v25
	v_mul_f32_e32 v20, 0xc01d265f, v20
	v_exp_f32_e32 v20, v20
	s_nop 0
	v_add_f32_e32 v20, 1.0, v20
	v_rcp_f32_e32 v20, v20
	s_nop 0
	v_mul_f32_e32 v25, v25, v20
	v_add_f32_e32 v20, v153, v3
	v_min_f32_e32 v20, 0x40e00000, v20
	v_mul_f32_e32 v26, v20, v26
	v_mul_f32_e32 v20, 0xc01d265f, v20
	v_exp_f32_e32 v20, v20
	s_nop 0
	v_add_f32_e32 v20, 1.0, v20
	v_rcp_f32_e32 v20, v20
	s_nop 0
	v_mul_f32_e32 v26, v26, v20
	v_add_f32_e32 v20, v154, v4
	v_min_f32_e32 v20, 0x40e00000, v20
	v_mul_f32_e32 v27, v20, v27
	v_mul_f32_e32 v20, 0xc01d265f, v20
	v_exp_f32_e32 v20, v20
	s_nop 0
	v_add_f32_e32 v20, 1.0, v20
	v_rcp_f32_e32 v20, v20
	s_nop 0
	v_mul_f32_e32 v27, v27, v20
	v_add_f32_e32 v20, v155, v5
	v_min_f32_e32 v20, 0x40e00000, v20
	v_mul_f32_e32 v28, v20, v28
	v_mul_f32_e32 v20, 0xc01d265f, v20
	v_exp_f32_e32 v20, v20
	s_nop 0
	v_add_f32_e32 v20, 1.0, v20
	v_rcp_f32_e32 v20, v20
	s_nop 0
	v_mul_f32_e32 v28, v28, v20
	v_mov_b32_e32 v20, v99
	v_cvt_pk_fp8_f32 v20, v21, v22
	v_mov_b32_e32 v21, v99
	v_cvt_pk_fp8_f32 v21, v25, v26
	v_add_co_u32_e32 v22, vcc, s10, v18
	v_cvt_pk_fp8_f32 v20, v23, v24 op_sel:[0,0,1]
	v_cvt_pk_fp8_f32 v21, v27, v28 op_sel:[0,0,1]
	v_addc_co_u32_e32 v23, vcc, 0, v19, vcc
	v_add_f32_e32 v24, v143, v17
	global_store_dwordx2 v[22:23], v[20:21], off
	v_add_f32_e32 v21, v140, v14
	v_add_f32_e32 v20, v144, v10
	v_med3_f32 v21, v21, s26, v236
	v_min_f32_e32 v20, 0x40e00000, v20
	v_add_f32_e32 v21, 1.0, v21
	v_mul_f32_e32 v21, v20, v21
	v_mul_f32_e32 v20, 0xc01d265f, v20
	v_exp_f32_e32 v20, v20
	v_add_f32_e32 v22, v141, v15
	v_med3_f32 v22, v22, s26, v236
	v_add_f32_e32 v22, 1.0, v22
	v_add_f32_e32 v20, 1.0, v20
	v_rcp_f32_e32 v20, v20
	v_add_f32_e32 v23, v142, v16
	v_med3_f32 v23, v23, s26, v236
	v_add_f32_e32 v23, 1.0, v23
	v_mul_f32_e32 v21, v21, v20
	v_add_f32_e32 v20, v145, v11
	v_min_f32_e32 v20, 0x40e00000, v20
	v_mul_f32_e32 v22, v20, v22
	v_mul_f32_e32 v20, 0xc01d265f, v20
	v_exp_f32_e32 v20, v20
	v_med3_f32 v24, v24, s26, v236
	v_add_f32_e32 v24, 1.0, v24
	v_add_f32_e32 v25, v132, v6
	v_add_f32_e32 v20, 1.0, v20
	v_rcp_f32_e32 v20, v20
	v_med3_f32 v25, v25, s26, v236
	v_add_f32_e32 v25, 1.0, v25
	v_add_f32_e32 v26, v133, v7
	v_mul_f32_e32 v22, v22, v20
	v_add_f32_e32 v20, v146, v12
	v_min_f32_e32 v20, 0x40e00000, v20
	v_mul_f32_e32 v23, v20, v23
	v_mul_f32_e32 v20, 0xc01d265f, v20
	v_exp_f32_e32 v20, v20
	v_med3_f32 v26, v26, s26, v236
	v_add_f32_e32 v26, 1.0, v26
	v_add_f32_e32 v27, v134, v8
	v_add_f32_e32 v20, 1.0, v20
	v_rcp_f32_e32 v20, v20
	v_med3_f32 v27, v27, s26, v236
	v_add_f32_e32 v27, 1.0, v27
	v_add_f32_e32 v28, v135, v9
	v_mul_f32_e32 v23, v23, v20
	v_add_f32_e32 v20, v147, v13
	v_min_f32_e32 v20, 0x40e00000, v20
	v_mul_f32_e32 v24, v20, v24
	v_mul_f32_e32 v20, 0xc01d265f, v20
	v_exp_f32_e32 v20, v20
	v_med3_f32 v28, v28, s26, v236
	v_add_f32_e32 v28, 1.0, v28
	s_mov_b32 s10, 0xc000
	v_add_f32_e32 v20, 1.0, v20
	v_rcp_f32_e32 v20, v20
	s_nop 0
	v_mul_f32_e32 v24, v24, v20
	v_add_f32_e32 v20, v136, v2
	v_min_f32_e32 v20, 0x40e00000, v20
	v_mul_f32_e32 v25, v20, v25
	v_mul_f32_e32 v20, 0xc01d265f, v20
	v_exp_f32_e32 v20, v20
	s_nop 0
	v_add_f32_e32 v20, 1.0, v20
	v_rcp_f32_e32 v20, v20
	s_nop 0
	v_mul_f32_e32 v25, v25, v20
	v_add_f32_e32 v20, v137, v3
	v_min_f32_e32 v20, 0x40e00000, v20
	v_mul_f32_e32 v26, v20, v26
	v_mul_f32_e32 v20, 0xc01d265f, v20
	v_exp_f32_e32 v20, v20
	s_nop 0
	v_add_f32_e32 v20, 1.0, v20
	v_rcp_f32_e32 v20, v20
	s_nop 0
	v_mul_f32_e32 v26, v26, v20
	v_add_f32_e32 v20, v138, v4
	v_min_f32_e32 v20, 0x40e00000, v20
	v_mul_f32_e32 v27, v20, v27
	v_mul_f32_e32 v20, 0xc01d265f, v20
	v_exp_f32_e32 v20, v20
	s_nop 0
	v_add_f32_e32 v20, 1.0, v20
	v_rcp_f32_e32 v20, v20
	s_nop 0
	v_mul_f32_e32 v27, v27, v20
	v_add_f32_e32 v20, v139, v5
	v_min_f32_e32 v20, 0x40e00000, v20
	v_mul_f32_e32 v28, v20, v28
	v_mul_f32_e32 v20, 0xc01d265f, v20
	v_exp_f32_e32 v20, v20
	s_nop 0
	v_add_f32_e32 v20, 1.0, v20
	v_rcp_f32_e32 v20, v20
	s_nop 0
	v_mul_f32_e32 v28, v28, v20
	v_mov_b32_e32 v20, v99
	v_cvt_pk_fp8_f32 v20, v21, v22
	v_mov_b32_e32 v21, v99
	v_cvt_pk_fp8_f32 v21, v25, v26
	v_add_co_u32_e32 v22, vcc, s10, v18
	v_cvt_pk_fp8_f32 v20, v23, v24 op_sel:[0,0,1]
	v_cvt_pk_fp8_f32 v21, v27, v28 op_sel:[0,0,1]
	v_addc_co_u32_e32 v23, vcc, 0, v19, vcc
	v_add_f32_e32 v24, v127, v17
	global_store_dwordx2 v[22:23], v[20:21], off
	v_add_f32_e32 v21, v124, v14
	v_add_f32_e32 v20, v128, v10
	v_med3_f32 v21, v21, s26, v236
	v_min_f32_e32 v20, 0x40e00000, v20
	v_add_f32_e32 v21, 1.0, v21
	v_mul_f32_e32 v21, v20, v21
	v_mul_f32_e32 v20, 0xc01d265f, v20
	v_exp_f32_e32 v20, v20
	v_add_f32_e32 v22, v125, v15
	v_med3_f32 v22, v22, s26, v236
	v_add_f32_e32 v22, 1.0, v22
	v_add_f32_e32 v20, 1.0, v20
	v_rcp_f32_e32 v20, v20
	v_add_f32_e32 v23, v126, v16
	v_med3_f32 v23, v23, s26, v236
	v_add_f32_e32 v23, 1.0, v23
	v_mul_f32_e32 v21, v21, v20
	v_add_f32_e32 v20, v129, v11
	v_min_f32_e32 v20, 0x40e00000, v20
	v_mul_f32_e32 v22, v20, v22
	v_mul_f32_e32 v20, 0xc01d265f, v20
	v_exp_f32_e32 v20, v20
	v_med3_f32 v24, v24, s26, v236
	v_add_f32_e32 v24, 1.0, v24
	v_add_f32_e32 v25, v116, v6
	v_add_f32_e32 v20, 1.0, v20
	v_rcp_f32_e32 v20, v20
	v_med3_f32 v25, v25, s26, v236
	v_add_f32_e32 v25, 1.0, v25
	v_add_f32_e32 v26, v117, v7
	v_mul_f32_e32 v22, v22, v20
	v_add_f32_e32 v20, v130, v12
	v_min_f32_e32 v20, 0x40e00000, v20
	v_mul_f32_e32 v23, v20, v23
	v_mul_f32_e32 v20, 0xc01d265f, v20
	v_exp_f32_e32 v20, v20
	v_med3_f32 v26, v26, s26, v236
	v_add_f32_e32 v26, 1.0, v26
	v_add_f32_e32 v27, v118, v8
	v_add_f32_e32 v20, 1.0, v20
	v_rcp_f32_e32 v20, v20
	v_med3_f32 v27, v27, s26, v236
	v_add_f32_e32 v27, 1.0, v27
	v_add_f32_e32 v28, v119, v9
	v_mul_f32_e32 v23, v23, v20
	v_add_f32_e32 v20, v131, v13
	v_min_f32_e32 v20, 0x40e00000, v20
	v_mul_f32_e32 v24, v20, v24
	v_mul_f32_e32 v20, 0xc01d265f, v20
	v_exp_f32_e32 v20, v20
	v_med3_f32 v28, v28, s26, v236
	v_add_f32_e32 v28, 1.0, v28
	s_mov_b32 s10, 0x20000
	v_add_f32_e32 v20, 1.0, v20
	v_rcp_f32_e32 v20, v20
	s_nop 0
	v_mul_f32_e32 v24, v24, v20
	v_add_f32_e32 v20, v120, v2
	v_min_f32_e32 v20, 0x40e00000, v20
	v_mul_f32_e32 v25, v20, v25
	v_mul_f32_e32 v20, 0xc01d265f, v20
	v_exp_f32_e32 v20, v20
	s_nop 0
	v_add_f32_e32 v20, 1.0, v20
	v_rcp_f32_e32 v20, v20
	s_nop 0
	v_mul_f32_e32 v25, v25, v20
	v_add_f32_e32 v20, v121, v3
	v_min_f32_e32 v20, 0x40e00000, v20
	v_mul_f32_e32 v26, v20, v26
	v_mul_f32_e32 v20, 0xc01d265f, v20
	v_exp_f32_e32 v20, v20
	s_nop 0
	v_add_f32_e32 v20, 1.0, v20
	v_rcp_f32_e32 v20, v20
	s_nop 0
	v_mul_f32_e32 v26, v26, v20
	v_add_f32_e32 v20, v122, v4
	v_min_f32_e32 v20, 0x40e00000, v20
	v_mul_f32_e32 v27, v20, v27
	v_mul_f32_e32 v20, 0xc01d265f, v20
	v_exp_f32_e32 v20, v20
	s_nop 0
	v_add_f32_e32 v20, 1.0, v20
	v_rcp_f32_e32 v20, v20
	s_nop 0
	v_mul_f32_e32 v27, v27, v20
	v_add_f32_e32 v20, v123, v5
	v_min_f32_e32 v20, 0x40e00000, v20
	v_mul_f32_e32 v28, v20, v28
	v_mul_f32_e32 v20, 0xc01d265f, v20
	v_exp_f32_e32 v20, v20
	s_nop 0
	v_add_f32_e32 v20, 1.0, v20
	v_rcp_f32_e32 v20, v20
	s_nop 0
	v_mul_f32_e32 v28, v28, v20
	v_mov_b32_e32 v20, v99
	v_cvt_pk_fp8_f32 v20, v21, v22
	v_mov_b32_e32 v21, v99
	v_cvt_pk_fp8_f32 v21, v25, v26
	v_add_co_u32_e32 v22, vcc, s10, v18
	v_cvt_pk_fp8_f32 v20, v23, v24 op_sel:[0,0,1]
	v_cvt_pk_fp8_f32 v21, v27, v28 op_sel:[0,0,1]
	v_addc_co_u32_e32 v23, vcc, 0, v19, vcc
	v_add_f32_e32 v24, v111, v17
	global_store_dwordx2 v[22:23], v[20:21], off
	v_add_f32_e32 v21, v108, v14
	v_add_f32_e32 v20, v112, v10
	v_med3_f32 v21, v21, s26, v236
	v_min_f32_e32 v20, 0x40e00000, v20
	v_add_f32_e32 v21, 1.0, v21
	v_mul_f32_e32 v21, v20, v21
	v_mul_f32_e32 v20, 0xc01d265f, v20
	v_exp_f32_e32 v20, v20
	v_add_f32_e32 v22, v109, v15
	v_med3_f32 v22, v22, s26, v236
	v_add_f32_e32 v22, 1.0, v22
	v_add_f32_e32 v20, 1.0, v20
	v_rcp_f32_e32 v20, v20
	v_add_f32_e32 v23, v110, v16
	v_med3_f32 v23, v23, s26, v236
	v_add_f32_e32 v23, 1.0, v23
	v_mul_f32_e32 v21, v21, v20
	v_add_f32_e32 v20, v113, v11
	v_min_f32_e32 v20, 0x40e00000, v20
	v_mul_f32_e32 v22, v20, v22
	v_mul_f32_e32 v20, 0xc01d265f, v20
	v_exp_f32_e32 v20, v20
	v_med3_f32 v24, v24, s26, v236
	v_add_f32_e32 v24, 1.0, v24
	v_add_f32_e32 v25, v100, v6
	v_add_f32_e32 v20, 1.0, v20
	v_rcp_f32_e32 v20, v20
	v_med3_f32 v25, v25, s26, v236
	v_add_f32_e32 v25, 1.0, v25
	v_add_f32_e32 v26, v101, v7
	v_mul_f32_e32 v22, v22, v20
	v_add_f32_e32 v20, v114, v12
	v_min_f32_e32 v20, 0x40e00000, v20
	v_mul_f32_e32 v23, v20, v23
	v_mul_f32_e32 v20, 0xc01d265f, v20
	v_exp_f32_e32 v20, v20
	v_med3_f32 v26, v26, s26, v236
	v_add_f32_e32 v26, 1.0, v26
	v_add_f32_e32 v27, v102, v8
	v_add_f32_e32 v20, 1.0, v20
	v_rcp_f32_e32 v20, v20
	v_med3_f32 v27, v27, s26, v236
	v_add_f32_e32 v27, 1.0, v27
	v_add_f32_e32 v28, v103, v9
	v_mul_f32_e32 v23, v23, v20
	v_add_f32_e32 v20, v115, v13
	v_min_f32_e32 v20, 0x40e00000, v20
	v_mul_f32_e32 v24, v20, v24
	v_mul_f32_e32 v20, 0xc01d265f, v20
	v_exp_f32_e32 v20, v20
	v_med3_f32 v28, v28, s26, v236
	v_add_f32_e32 v28, 1.0, v28
	s_mov_b32 s10, 0x24000
	v_add_f32_e32 v20, 1.0, v20
	v_rcp_f32_e32 v20, v20
	s_nop 0
	v_mul_f32_e32 v24, v24, v20
	v_add_f32_e32 v20, v104, v2
	v_min_f32_e32 v20, 0x40e00000, v20
	v_mul_f32_e32 v25, v20, v25
	v_mul_f32_e32 v20, 0xc01d265f, v20
	v_exp_f32_e32 v20, v20
	s_nop 0
	v_add_f32_e32 v20, 1.0, v20
	v_rcp_f32_e32 v20, v20
	s_nop 0
	v_mul_f32_e32 v25, v25, v20
	v_add_f32_e32 v20, v105, v3
	v_min_f32_e32 v20, 0x40e00000, v20
	v_mul_f32_e32 v26, v20, v26
	v_mul_f32_e32 v20, 0xc01d265f, v20
	v_exp_f32_e32 v20, v20
	s_nop 0
	v_add_f32_e32 v20, 1.0, v20
	v_rcp_f32_e32 v20, v20
	s_nop 0
	v_mul_f32_e32 v26, v26, v20
	v_add_f32_e32 v20, v106, v4
	v_min_f32_e32 v20, 0x40e00000, v20
	v_mul_f32_e32 v27, v20, v27
	v_mul_f32_e32 v20, 0xc01d265f, v20
	v_exp_f32_e32 v20, v20
	s_nop 0
	v_add_f32_e32 v20, 1.0, v20
	v_rcp_f32_e32 v20, v20
	s_nop 0
	v_mul_f32_e32 v27, v27, v20
	v_add_f32_e32 v20, v107, v5
	v_min_f32_e32 v20, 0x40e00000, v20
	v_mul_f32_e32 v28, v20, v28
	v_mul_f32_e32 v20, 0xc01d265f, v20
	v_exp_f32_e32 v20, v20
	s_nop 0
	v_add_f32_e32 v20, 1.0, v20
	v_rcp_f32_e32 v20, v20
	s_nop 0
	v_mul_f32_e32 v28, v28, v20
	v_mov_b32_e32 v20, v99
	v_cvt_pk_fp8_f32 v20, v21, v22
	v_mov_b32_e32 v21, v99
	v_cvt_pk_fp8_f32 v21, v25, v26
	v_add_co_u32_e32 v22, vcc, s10, v18
	v_cvt_pk_fp8_f32 v20, v23, v24 op_sel:[0,0,1]
	v_cvt_pk_fp8_f32 v21, v27, v28 op_sel:[0,0,1]
	v_addc_co_u32_e32 v23, vcc, 0, v19, vcc
	v_add_f32_e32 v24, v93, v17
	global_store_dwordx2 v[22:23], v[20:21], off
	v_add_f32_e32 v21, v90, v14
	v_add_f32_e32 v20, v94, v10
	v_med3_f32 v21, v21, s26, v236
	v_min_f32_e32 v20, 0x40e00000, v20
	v_add_f32_e32 v21, 1.0, v21
	v_mul_f32_e32 v21, v20, v21
	v_mul_f32_e32 v20, 0xc01d265f, v20
	v_exp_f32_e32 v20, v20
	v_add_f32_e32 v22, v91, v15
	v_med3_f32 v22, v22, s26, v236
	v_add_f32_e32 v22, 1.0, v22
	v_add_f32_e32 v20, 1.0, v20
	v_rcp_f32_e32 v20, v20
	v_add_f32_e32 v23, v92, v16
	v_med3_f32 v23, v23, s26, v236
	v_add_f32_e32 v23, 1.0, v23
	v_mul_f32_e32 v21, v21, v20
	v_add_f32_e32 v20, v95, v11
	v_min_f32_e32 v20, 0x40e00000, v20
	v_mul_f32_e32 v22, v20, v22
	v_mul_f32_e32 v20, 0xc01d265f, v20
	v_exp_f32_e32 v20, v20
	v_med3_f32 v24, v24, s26, v236
	v_add_f32_e32 v24, 1.0, v24
	v_add_f32_e32 v25, v82, v6
	v_add_f32_e32 v20, 1.0, v20
	v_rcp_f32_e32 v20, v20
	v_add_f32_e32 v6, v66, v6
	v_med3_f32 v25, v25, s26, v236
	v_med3_f32 v6, v6, s26, v236
	v_mul_f32_e32 v22, v22, v20
	v_add_f32_e32 v20, v96, v12
	v_min_f32_e32 v20, 0x40e00000, v20
	v_mul_f32_e32 v23, v20, v23
	v_mul_f32_e32 v20, 0xc01d265f, v20
	v_exp_f32_e32 v20, v20
	v_add_f32_e32 v25, 1.0, v25
	v_add_f32_e32 v6, 1.0, v6
	v_add_f32_e32 v14, v74, v14
	v_add_f32_e32 v20, 1.0, v20
	v_rcp_f32_e32 v20, v20
	v_add_f32_e32 v10, v78, v10
	v_med3_f32 v14, v14, s26, v236
	v_min_f32_e32 v10, 0x40e00000, v10
	v_mul_f32_e32 v23, v23, v20
	v_add_f32_e32 v20, v97, v13
	v_min_f32_e32 v20, 0x40e00000, v20
	v_mul_f32_e32 v24, v20, v24
	v_mul_f32_e32 v20, 0xc01d265f, v20
	v_exp_f32_e32 v20, v20
	v_add_f32_e32 v14, 1.0, v14
	v_mul_f32_e32 v14, v10, v14
	v_mul_f32_e32 v10, 0xc01d265f, v10
	v_add_f32_e32 v20, 1.0, v20
	v_rcp_f32_e32 v20, v20
	v_exp_f32_e32 v10, v10
	v_add_f32_e32 v26, v83, v7
	v_med3_f32 v26, v26, s26, v236
	v_mul_f32_e32 v24, v24, v20
	v_add_f32_e32 v20, v86, v2
	v_add_f32_e32 v2, v70, v2
	v_min_f32_e32 v20, 0x40e00000, v20
	v_min_f32_e32 v2, 0x40e00000, v2
	v_mul_f32_e32 v25, v20, v25
	v_mul_f32_e32 v20, 0xc01d265f, v20
	v_mul_f32_e32 v6, v2, v6
	v_mul_f32_e32 v2, 0xc01d265f, v2
	v_exp_f32_e32 v20, v20
	v_exp_f32_e32 v2, v2
	v_add_f32_e32 v10, 1.0, v10
	v_rcp_f32_e32 v10, v10
	v_add_f32_e32 v20, 1.0, v20
	v_add_f32_e32 v2, 1.0, v2
	v_rcp_f32_e32 v20, v20
	v_rcp_f32_e32 v2, v2
	v_add_f32_e32 v26, 1.0, v26
	v_mul_f32_e32 v10, v14, v10
	v_mul_f32_e32 v25, v25, v20
	v_add_f32_e32 v20, v87, v3
	v_mul_f32_e32 v6, v6, v2
	v_add_f32_e32 v2, v71, v3
	v_add_f32_e32 v3, v67, v7
	v_med3_f32 v3, v3, s26, v236
	v_min_f32_e32 v2, 0x40e00000, v2
	v_add_f32_e32 v3, 1.0, v3
	v_min_f32_e32 v20, 0x40e00000, v20
	v_mul_f32_e32 v3, v2, v3
	v_mul_f32_e32 v2, 0xc01d265f, v2
	v_mul_f32_e32 v26, v20, v26
	v_mul_f32_e32 v20, 0xc01d265f, v20
	v_add_f32_e32 v14, v75, v15
	v_exp_f32_e32 v2, v2
	v_exp_f32_e32 v20, v20
	v_add_f32_e32 v11, v79, v11
	v_med3_f32 v14, v14, s26, v236
	v_min_f32_e32 v11, 0x40e00000, v11
	v_add_f32_e32 v14, 1.0, v14
	v_mul_f32_e32 v14, v11, v14
	v_mul_f32_e32 v11, 0xc01d265f, v11
	v_exp_f32_e32 v11, v11
	v_add_f32_e32 v2, 1.0, v2
	v_add_f32_e32 v20, 1.0, v20
	v_rcp_f32_e32 v2, v2
	v_rcp_f32_e32 v20, v20
	v_add_f32_e32 v11, 1.0, v11
	v_add_f32_e32 v27, v84, v8
	v_rcp_f32_e32 v11, v11
	v_mul_f32_e32 v7, v3, v2
	v_add_f32_e32 v3, v68, v8
	v_mul_f32_e32 v26, v26, v20
	v_add_f32_e32 v20, v88, v4
	v_med3_f32 v27, v27, s26, v236
	v_add_f32_e32 v2, v72, v4
	v_med3_f32 v3, v3, s26, v236
	v_min_f32_e32 v20, 0x40e00000, v20
	v_add_f32_e32 v27, 1.0, v27
	v_min_f32_e32 v2, 0x40e00000, v2
	v_add_f32_e32 v3, 1.0, v3
	v_mul_f32_e32 v27, v20, v27
	v_mul_f32_e32 v20, 0xc01d265f, v20
	v_mul_f32_e32 v3, v2, v3
	v_mul_f32_e32 v2, 0xc01d265f, v2
	v_exp_f32_e32 v20, v20
	v_mul_f32_e32 v11, v14, v11
	v_add_f32_e32 v14, v76, v16
	v_exp_f32_e32 v2, v2
	v_add_f32_e32 v12, v80, v12
	v_med3_f32 v14, v14, s26, v236
	v_min_f32_e32 v12, 0x40e00000, v12
	v_add_f32_e32 v14, 1.0, v14
	v_mul_f32_e32 v14, v12, v14
	v_mul_f32_e32 v12, 0xc01d265f, v12
	v_add_f32_e32 v20, 1.0, v20
	v_exp_f32_e32 v12, v12
	v_add_f32_e32 v2, 1.0, v2
	v_rcp_f32_e32 v20, v20
	v_rcp_f32_e32 v2, v2
	v_add_f32_e32 v28, v85, v9
	v_add_f32_e32 v12, 1.0, v12
	v_mul_f32_e32 v27, v27, v20
	v_add_f32_e32 v20, v89, v5
	v_med3_f32 v28, v28, s26, v236
	v_rcp_f32_e32 v12, v12
	v_mul_f32_e32 v4, v3, v2
	v_add_f32_e32 v3, v69, v9
	v_min_f32_e32 v20, 0x40e00000, v20
	v_add_f32_e32 v28, 1.0, v28
	v_add_f32_e32 v2, v73, v5
	v_med3_f32 v3, v3, s26, v236
	v_mul_f32_e32 v28, v20, v28
	v_mul_f32_e32 v20, 0xc01d265f, v20
	v_min_f32_e32 v2, 0x40e00000, v2
	v_add_f32_e32 v3, 1.0, v3
	v_exp_f32_e32 v20, v20
	v_mul_f32_e32 v3, v2, v3
	v_mul_f32_e32 v2, 0xc01d265f, v2
	v_mul_f32_e32 v12, v14, v12
	v_add_f32_e32 v14, v77, v17
	v_exp_f32_e32 v2, v2
	v_add_f32_e32 v13, v81, v13
	v_med3_f32 v14, v14, s26, v236
	v_min_f32_e32 v13, 0x40e00000, v13
	v_add_f32_e32 v14, 1.0, v14
	v_add_f32_e32 v20, 1.0, v20
	v_mul_f32_e32 v14, v13, v14
	v_mul_f32_e32 v13, 0xc01d265f, v13
	v_rcp_f32_e32 v20, v20
	v_exp_f32_e32 v13, v13
	v_add_f32_e32 v2, 1.0, v2
	v_rcp_f32_e32 v2, v2
	v_mul_f32_e32 v28, v28, v20
	v_mov_b32_e32 v20, v99
	v_add_f32_e32 v13, 1.0, v13
	v_cvt_pk_fp8_f32 v20, v21, v22
	v_mov_b32_e32 v21, v99
	v_rcp_f32_e32 v13, v13
	v_mul_f32_e32 v5, v3, v2
	v_mov_b32_e32 v2, v99
	v_mov_b32_e32 v3, v99
	v_cvt_pk_fp8_f32 v21, v25, v26
	v_cvt_pk_fp8_f32 v2, v10, v11
	v_cvt_pk_fp8_f32 v3, v6, v7
	s_mov_b32 s10, 0x28000
	v_add_co_u32_e32 v22, vcc, s10, v18
	v_mul_f32_e32 v13, v14, v13
	v_cvt_pk_fp8_f32 v20, v23, v24 op_sel:[0,0,1]
	v_cvt_pk_fp8_f32 v21, v27, v28 op_sel:[0,0,1]
	v_addc_co_u32_e32 v23, vcc, 0, v19, vcc
	v_cvt_pk_fp8_f32 v2, v12, v13 op_sel:[0,0,1]
	v_cvt_pk_fp8_f32 v3, v4, v5 op_sel:[0,0,1]
	v_add_co_u32_e32 v4, vcc, 0x2c000, v18
	s_mov_b64 s[10:11], -1
	s_nop 0
	v_addc_co_u32_e32 v5, vcc, 0, v19, vcc
	s_andn2_b64 vcc, exec, s[8:9]
	global_store_dwordx2 v[22:23], v[20:21], off
	global_store_dwordx2 v[4:5], v[2:3], off
	s_cbranch_vccnz .LBB0_1427
	s_andn2_b64 vcc, exec, s[4:5]
	s_cbranch_vccnz .LBB0_1426
	s_barrier
	s_branch .LBB0_1426
